# scan loader: V/gate/chunk-total loads also issued one chunk ahead (end of window B)
# baseline (speedup 1.0000x reference)
; __device__ __forceinline__ void p4_scan(const Args& a, const Frame& F) {
;     ...
;             auto conv_load = [&](int it) {
;                 const float* cW; int cN, cn;
;                 if (it < 32768) { const int e = it >> 10, sb = it & 1023; ck0 = (sb >> 6) * 64; cn = (sb & 63) * 32 + (lane & 31); cN = 2048; cW = a.in[IN_W1] + (size_t)e * 1024 * 2048; cD = (bf16*)(a.ws + WS_W1T);
;                     const int up = cn >= 1024, nn = cn & 1023; crow = e * 2048 + (nn >> 7) * 256 + up * 128 + (nn & 127); }
;                 else { const int it2 = it - 32768, e = it2 >> 9, sb = it2 & 511; ck0 = (sb >> 5) * 64; cn = (sb & 31) * 32 + (lane & 31); cN = 1024; cW = a.in[IN_W2] + (size_t)e * 1024 * 1024; cD = (bf16*)(a.ws + WS_W2T); crow = e * 1024 + cn; }
; #pragma unroll
;                 for (int i = 0; i < 32; ++i) cv[i] = cW[(size_t)(ck0 + (lane >> 5) + 2 * i) * cN + cn];
;             };
.LBB0_490:
	v_and_b32_e32 v82, 0x3c0, v9
	v_or_b32_e32 v14, v82, v158
	v_mov_b32_e32 v9, v145
	v_mul_u32_u24_e32 v12, s54, v14
	v_lshl_add_u64 v[8:9], v[8:9], 2, s[56:57]
	v_lshlrev_b32_e32 v12, 2, v12
	v_mov_b32_e32 v13, v145
	v_lshl_add_u64 v[12:13], v[8:9], 0, v[12:13]
	global_load_dword v148, v[12:13], off
	v_or_b32_e32 v12, 2, v14
	v_mul_u32_u24_e32 v12, s54, v12
	v_lshlrev_b32_e32 v12, 2, v12
	v_mov_b32_e32 v13, v145
	v_lshl_add_u64 v[12:13], v[8:9], 0, v[12:13]
	global_load_dword v141, v[12:13], off
	v_or_b32_e32 v12, 4, v14
	v_mul_u32_u24_e32 v12, s54, v12
	v_lshlrev_b32_e32 v12, 2, v12
	v_mov_b32_e32 v13, v145
	v_lshl_add_u64 v[12:13], v[8:9], 0, v[12:13]
	global_load_dword v149, v[12:13], off
	v_or_b32_e32 v12, 6, v14
	v_mul_u32_u24_e32 v12, s54, v12
	v_lshlrev_b32_e32 v12, 2, v12
	v_mov_b32_e32 v13, v145
	v_lshl_add_u64 v[12:13], v[8:9], 0, v[12:13]
	global_load_dword v137, v[12:13], off
	v_or_b32_e32 v12, 8, v14
	v_mul_u32_u24_e32 v12, s54, v12
	v_lshlrev_b32_e32 v12, 2, v12
	v_mov_b32_e32 v13, v145
	v_lshl_add_u64 v[12:13], v[8:9], 0, v[12:13]
	global_load_dword v142, v[12:13], off
	v_or_b32_e32 v12, 10, v14
	v_mul_u32_u24_e32 v12, s54, v12
	v_lshlrev_b32_e32 v12, 2, v12
	v_mov_b32_e32 v13, v145
	v_lshl_add_u64 v[12:13], v[8:9], 0, v[12:13]
	global_load_dword v81, v[12:13], off
	v_or_b32_e32 v12, 12, v14
	v_mul_u32_u24_e32 v12, s54, v12
	v_lshlrev_b32_e32 v12, 2, v12
	v_mov_b32_e32 v13, v145
	v_lshl_add_u64 v[12:13], v[8:9], 0, v[12:13]
	global_load_dword v138, v[12:13], off
	v_or_b32_e32 v12, 14, v14
	v_mul_u32_u24_e32 v12, s54, v12
	v_lshlrev_b32_e32 v12, 2, v12
	v_mov_b32_e32 v13, v145
	v_lshl_add_u64 v[12:13], v[8:9], 0, v[12:13]
	global_load_dword v151, v[12:13], off
	v_or_b32_e32 v12, 16, v14
	v_mul_u32_u24_e32 v12, s54, v12
	v_lshlrev_b32_e32 v12, 2, v12
	v_mov_b32_e32 v13, v145
	v_lshl_add_u64 v[12:13], v[8:9], 0, v[12:13]
	global_load_dword v152, v[12:13], off
	v_or_b32_e32 v12, 18, v14
	v_mul_u32_u24_e32 v12, s54, v12
	v_lshlrev_b32_e32 v12, 2, v12
	v_mov_b32_e32 v13, v145
	v_lshl_add_u64 v[12:13], v[8:9], 0, v[12:13]
	global_load_dword v143, v[12:13], off
	v_or_b32_e32 v12, 20, v14
	v_mul_u32_u24_e32 v12, s54, v12
	v_lshlrev_b32_e32 v12, 2, v12
	v_mov_b32_e32 v13, v145
	v_lshl_add_u64 v[12:13], v[8:9], 0, v[12:13]
	global_load_dword v150, v[12:13], off
	v_or_b32_e32 v12, 22, v14
	v_mul_u32_u24_e32 v12, s54, v12
	v_lshlrev_b32_e32 v12, 2, v12
	v_mov_b32_e32 v13, v145
	v_lshl_add_u64 v[12:13], v[8:9], 0, v[12:13]
	global_load_dword v139, v[12:13], off
	v_or_b32_e32 v12, 24, v14
	v_mul_u32_u24_e32 v12, s54, v12
	v_lshlrev_b32_e32 v12, 2, v12
	v_mov_b32_e32 v13, v145
	v_lshl_add_u64 v[12:13], v[8:9], 0, v[12:13]
	global_load_dword v147, v[12:13], off
	v_or_b32_e32 v12, 26, v14
	v_mul_u32_u24_e32 v12, s54, v12
	v_lshlrev_b32_e32 v12, 2, v12
	v_mov_b32_e32 v13, v145
	v_lshl_add_u64 v[12:13], v[8:9], 0, v[12:13]
	global_load_dword v83, v[12:13], off
	v_or_b32_e32 v12, 28, v14
	v_mul_u32_u24_e32 v12, s54, v12
	v_lshlrev_b32_e32 v12, 2, v12
	v_mov_b32_e32 v13, v145
	v_lshl_add_u64 v[12:13], v[8:9], 0, v[12:13]
	global_load_dword v140, v[12:13], off
	v_or_b32_e32 v12, 30, v14
	v_mul_u32_u24_e32 v12, s54, v12
	v_lshlrev_b32_e32 v12, 2, v12
	v_mov_b32_e32 v13, v145
	v_lshl_add_u64 v[12:13], v[8:9], 0, v[12:13]
	global_load_dword v153, v[12:13], off
	v_or_b32_e32 v12, 32, v14
	v_mul_u32_u24_e32 v12, s54, v12
	v_lshlrev_b32_e32 v12, 2, v12
	v_mov_b32_e32 v13, v145
	v_lshl_add_u64 v[12:13], v[8:9], 0, v[12:13]
	global_load_dword v183, v[12:13], off
	v_or_b32_e32 v12, 34, v14
	v_mul_u32_u24_e32 v12, s54, v12
	v_lshlrev_b32_e32 v12, 2, v12
	v_mov_b32_e32 v13, v145
	v_lshl_add_u64 v[12:13], v[8:9], 0, v[12:13]
	global_load_dword v179, v[12:13], off
	v_or_b32_e32 v12, 36, v14
	v_mul_u32_u24_e32 v12, s54, v12
	v_lshlrev_b32_e32 v12, 2, v12
	v_mov_b32_e32 v13, v145
	v_lshl_add_u64 v[12:13], v[8:9], 0, v[12:13]
	global_load_dword v184, v[12:13], off
	v_or_b32_e32 v12, 38, v14
	v_mul_u32_u24_e32 v12, s54, v12
	v_lshlrev_b32_e32 v12, 2, v12
	v_mov_b32_e32 v13, v145
	v_lshl_add_u64 v[12:13], v[8:9], 0, v[12:13]
	global_load_dword v175, v[12:13], off
	v_or_b32_e32 v12, 40, v14
	v_mul_u32_u24_e32 v12, s54, v12
	v_lshlrev_b32_e32 v12, 2, v12
	v_mov_b32_e32 v13, v145
	v_lshl_add_u64 v[12:13], v[8:9], 0, v[12:13]
	global_load_dword v180, v[12:13], off
	v_or_b32_e32 v12, 42, v14
	v_mul_u32_u24_e32 v12, s54, v12
	v_lshlrev_b32_e32 v12, 2, v12
	v_mov_b32_e32 v13, v145
	v_lshl_add_u64 v[12:13], v[8:9], 0, v[12:13]
	global_load_dword v173, v[12:13], off
	v_or_b32_e32 v12, 44, v14
	v_mul_u32_u24_e32 v12, s54, v12
	v_lshlrev_b32_e32 v12, 2, v12
	v_mov_b32_e32 v13, v145
	v_lshl_add_u64 v[12:13], v[8:9], 0, v[12:13]
	global_load_dword v176, v[12:13], off
	v_or_b32_e32 v12, 46, v14
	v_mul_u32_u24_e32 v12, s54, v12
	v_lshlrev_b32_e32 v12, 2, v12
	v_mov_b32_e32 v13, v145
	v_lshl_add_u64 v[12:13], v[8:9], 0, v[12:13]
	global_load_dword v186, v[12:13], off
	v_or_b32_e32 v12, 48, v14
	v_mul_u32_u24_e32 v12, s54, v12
	v_lshlrev_b32_e32 v12, 2, v12
	v_mov_b32_e32 v13, v145
	v_lshl_add_u64 v[12:13], v[8:9], 0, v[12:13]
	global_load_dword v187, v[12:13], off
	v_or_b32_e32 v12, 50, v14
	v_mul_u32_u24_e32 v12, s54, v12
	v_lshlrev_b32_e32 v12, 2, v12
	v_mov_b32_e32 v13, v145
	v_lshl_add_u64 v[12:13], v[8:9], 0, v[12:13]
	global_load_dword v181, v[12:13], off
	v_or_b32_e32 v12, 52, v14
	v_mul_u32_u24_e32 v12, s54, v12
	v_lshlrev_b32_e32 v12, 2, v12
	v_mov_b32_e32 v13, v145
	v_lshl_add_u64 v[12:13], v[8:9], 0, v[12:13]
	global_load_dword v185, v[12:13], off
	v_or_b32_e32 v12, 54, v14
	v_mul_u32_u24_e32 v12, s54, v12
	v_lshlrev_b32_e32 v12, 2, v12
	v_mov_b32_e32 v13, v145
; __device__ __forceinline__ void p4_scan(const Args& a, const Frame& F) {
;     ...
;                 for (int i = 0; i < 8; ++i) { const int p = ht + 256 * i, row = p >> 4, c16 = p & 15; const int tok = base + (dir ? 127 - row : row);
;                     pq[i] = *(const u32x4*)(QKC + (size_t)tok * 1024 + h * 128 + c16 * 8); pk[i] = *(const u32x4*)(QKC + (size_t)tok * 1024 + 512 + h * 128 + c16 * 8); }
; #pragma unroll
;                 for (int i = 0; i < 2; ++i) { const int p = ht + 256 * i, row = p >> 2, cc = p & 3; const int tok = base + (dir ? 127 - row : row);
;                     pv[i] = *(const u32x4*)(PV + (size_t)tok * 512 + h * 128 + vs * 32 + cc * 8); pga[i] = GS[(size_t)hd * TA + tok]; }
; #pragma unroll
;                 for (int i = 0; i < 2; ++i) { const int idx = ht + 256 * i; if (idx < 384) { const int row = idx & 127, arr = idx >> 7; const int tok = base + (dir ? 127 - row : row); pgl[i] = GS[(size_t)(arr * 8 + hd) * TA + tok]; } }
;                 pbt = CH[(hd * 528 + (base >> 7)) * 2]; ppx = CH[(hd * 528 + (base >> 7)) * 2 + 1];
;     ...
;             auto conv_load = [&](int it) {
;                 const float* cW; int cN, cn;
;                 if (it < 32768) { const int e = it >> 10, sb = it & 1023; ck0 = (sb >> 6) * 64; cn = (sb & 63) * 32 + (lane & 31); cN = 2048; cW = a.in[IN_W1] + (size_t)e * 1024 * 2048; cD = (bf16*)(a.ws + WS_W1T);
;                     const int up = cn >= 1024, nn = cn & 1023; crow = e * 2048 + (nn >> 7) * 256 + up * 128 + (nn & 127); }
;                 else { const int it2 = it - 32768, e = it2 >> 9, sb = it2 & 511; ck0 = (sb >> 5) * 64; cn = (sb & 31) * 32 + (lane & 31); cN = 1024; cW = a.in[IN_W2] + (size_t)e * 1024 * 1024; cD = (bf16*)(a.ws + WS_W2T); crow = e * 1024 + cn; }
; #pragma unroll
;                 for (int i = 0; i < 32; ++i) cv[i] = cW[(size_t)(ck0 + (lane >> 5) + 2 * i) * cN + cn];
;             };
	v_lshl_add_u64 v[12:13], v[8:9], 0, v[12:13]
	global_load_dword v177, v[12:13], off
	v_or_b32_e32 v12, 56, v14
	v_mul_u32_u24_e32 v12, s54, v12
	v_lshlrev_b32_e32 v12, 2, v12
	v_mov_b32_e32 v13, v145
	v_lshl_add_u64 v[12:13], v[8:9], 0, v[12:13]
	global_load_dword v182, v[12:13], off
	v_or_b32_e32 v12, 58, v14
	v_mul_u32_u24_e32 v12, s54, v12
	v_lshlrev_b32_e32 v12, 2, v12
	v_mov_b32_e32 v13, v145
	v_lshl_add_u64 v[12:13], v[8:9], 0, v[12:13]
	global_load_dword v174, v[12:13], off
	v_or_b32_e32 v12, 60, v14
	v_mul_u32_u24_e32 v12, s54, v12
	v_lshlrev_b32_e32 v12, 2, v12
	v_mov_b32_e32 v13, v145
	v_lshl_add_u64 v[12:13], v[8:9], 0, v[12:13]
	global_load_dword v178, v[12:13], off
	v_or_b32_e32 v12, 62, v14
	v_mul_u32_u24_e32 v12, s54, v12
	v_lshlrev_b32_e32 v12, 2, v12
	v_mov_b32_e32 v13, v145
	v_lshl_add_u64 v[8:9], v[8:9], 0, v[12:13]
	global_load_dword v188, v[8:9], off
	s_lshl_b32 s44, s44, 1
	s_add_u32 s54, s20, s44
	s_addc_u32 s55, s21, 0
	s_lshl_b32 s33, s33, 1
	s_add_u32 s54, s54, s33
	s_addc_u32 s55, s55, 0
	v_mov_b32_e32 v87, v145
	v_lshl_add_u64 v[86:87], s[54:55], 0, v[86:87]
	s_add_i32 s54, s34, s35
	v_mov_b64_e32 v[8:9], s[38:39]
	s_add_i32 s33, 0, 0x23430
	v_mad_i64_i32 v[88:89], s[34:35], v88, s95, v[8:9]
	v_mad_i64_i32 v[90:91], s[34:35], v90, s95, v[8:9]
	s_add_i32 s54, s54, 0x10000
	v_add_u32_e32 v12, s33, v11
	s_lshl_b32 s33, s58, 13
	s_xor_b32 s34, s54, 0x80
	s_add_u32 s54, s16, s44
	v_add_u32_e32 v11, s89, v11
	s_addc_u32 s55, s17, 0
	v_lshl_add_u64 v[92:93], s[54:55], 0, v[144:145]
	s_mov_b32 s44, 0
	v_mov_b32_e32 v136, 0
	v_add_u32_e32 v134, v12, v10
	v_add_u32_e32 v135, v11, v10
	v_add_u32_e32 v214, s34, v96
	v_ashrrev_i32_e32 v215, 31, v214
	v_lshlrev_b64 v[214:215], 11, v[214:215]
	v_lshl_add_u64 v[214:215], v[92:93], 0, v[214:215]
	global_load_dwordx4 v[220:223], v[214:215], off offset:1024
	v_add_u32_e32 v214, s34, v97
	v_ashrrev_i32_e32 v215, 31, v214
	v_lshlrev_b64 v[214:215], 11, v[214:215]
	v_lshl_add_u64 v[214:215], v[92:93], 0, v[214:215]
	global_load_dwordx4 v[224:227], v[214:215], off offset:1024
	v_add_u32_e32 v214, s34, v98
	v_ashrrev_i32_e32 v215, 31, v214
	v_lshlrev_b64 v[214:215], 11, v[214:215]
	v_lshl_add_u64 v[214:215], v[92:93], 0, v[214:215]
	global_load_dwordx4 v[228:231], v[214:215], off offset:1024
	v_add_u32_e32 v214, s34, v99
	v_ashrrev_i32_e32 v215, 31, v214
	v_lshlrev_b64 v[214:215], 11, v[214:215]
	v_lshl_add_u64 v[214:215], v[92:93], 0, v[214:215]
	global_load_dwordx4 v[232:235], v[214:215], off offset:1024
	v_add_u32_e32 v214, s34, v100
	v_ashrrev_i32_e32 v215, 31, v214
	v_lshlrev_b64 v[214:215], 11, v[214:215]
	v_lshl_add_u64 v[214:215], v[92:93], 0, v[214:215]
	global_load_dwordx4 v[236:239], v[214:215], off offset:1024
	v_add_u32_e32 v214, s34, v101
	v_ashrrev_i32_e32 v215, 31, v214
	v_lshlrev_b64 v[214:215], 11, v[214:215]
	v_lshl_add_u64 v[214:215], v[92:93], 0, v[214:215]
	global_load_dwordx4 v[240:243], v[214:215], off offset:1024
	v_add_u32_e32 v214, s34, v102
	v_ashrrev_i32_e32 v215, 31, v214
	v_lshlrev_b64 v[214:215], 11, v[214:215]
	v_lshl_add_u64 v[214:215], v[92:93], 0, v[214:215]
	global_load_dwordx4 v[244:247], v[214:215], off offset:1024
	v_add_u32_e32 v214, s34, v103
	v_ashrrev_i32_e32 v215, 31, v214
	v_lshlrev_b64 v[214:215], 11, v[214:215]
	v_lshl_add_u64 v[214:215], v[92:93], 0, v[214:215]
	global_load_dwordx4 v[248:251], v[214:215], off offset:1024
	v_add_u32_e32 v214, s34, v96
	v_ashrrev_i32_e32 v215, 31, v214
	v_lshlrev_b64 v[214:215], 11, v[214:215]
	v_lshl_add_u64 v[214:215], v[92:93], 0, v[214:215]
	global_load_dwordx4 v[16:19], v[214:215], off
	v_add_u32_e32 v214, s34, v97
	v_ashrrev_i32_e32 v215, 31, v214
	v_lshlrev_b64 v[214:215], 11, v[214:215]
	v_lshl_add_u64 v[214:215], v[92:93], 0, v[214:215]
	global_load_dwordx4 v[20:23], v[214:215], off
	v_add_u32_e32 v214, s34, v98
	v_ashrrev_i32_e32 v215, 31, v214
	v_lshlrev_b64 v[214:215], 11, v[214:215]
	v_lshl_add_u64 v[214:215], v[92:93], 0, v[214:215]
	global_load_dwordx4 v[24:27], v[214:215], off
	v_add_u32_e32 v214, s34, v99
	v_ashrrev_i32_e32 v215, 31, v214
	v_lshlrev_b64 v[214:215], 11, v[214:215]
	v_lshl_add_u64 v[214:215], v[92:93], 0, v[214:215]
	global_load_dwordx4 v[28:31], v[214:215], off
	v_add_u32_e32 v214, s34, v100
	v_ashrrev_i32_e32 v215, 31, v214
	v_lshlrev_b64 v[214:215], 11, v[214:215]
	v_lshl_add_u64 v[214:215], v[92:93], 0, v[214:215]
	global_load_dwordx4 v[32:35], v[214:215], off
	v_add_u32_e32 v214, s34, v101
	v_ashrrev_i32_e32 v215, 31, v214
	v_lshlrev_b64 v[214:215], 11, v[214:215]
	v_lshl_add_u64 v[214:215], v[92:93], 0, v[214:215]
	global_load_dwordx4 v[36:39], v[214:215], off
	v_add_u32_e32 v214, s34, v102
	v_ashrrev_i32_e32 v215, 31, v214
	v_lshlrev_b64 v[214:215], 11, v[214:215]
	v_lshl_add_u64 v[214:215], v[92:93], 0, v[214:215]
	global_load_dwordx4 v[40:43], v[214:215], off
	v_add_u32_e32 v214, s34, v103
	v_ashrrev_i32_e32 v215, 31, v214
	v_lshlrev_b64 v[214:215], 11, v[214:215]
	v_lshl_add_u64 v[214:215], v[92:93], 0, v[214:215]
	global_load_dwordx4 v[44:47], v[214:215], off
	v_add_u32_e32 v8, s34, v104
	v_ashrrev_i32_e32 v9, 31, v8
	v_lshlrev_b64 v[10:11], 10, v[8:9]
	v_lshl_add_u64 v[10:11], v[86:87], 0, v[10:11]
	v_lshl_add_u64 v[8:9], v[8:9], 2, s[50:51]
	global_load_dwordx4 v[12:15], v[10:11], off
	global_load_dword v172, v[8:9], off
	v_add_u32_e32 v8, s34, v105
	v_ashrrev_i32_e32 v9, 31, v8
	v_lshlrev_b64 v[10:11], 10, v[8:9]
	v_lshl_add_u64 v[10:11], v[86:87], 0, v[10:11]
	v_lshl_add_u64 v[94:95], v[8:9], 2, s[50:51]
	global_load_dwordx4 v[8:11], v[10:11], off
	s_nop 0
	global_load_dword v171, v[94:95], off
	v_or_b32_e32 v94, s34, v106
	v_ashrrev_i32_e32 v95, 31, v94
	v_lshl_add_u64 v[190:191], v[94:95], 2, v[88:89]
	global_load_dword v108, v[190:191], off
	v_lshl_add_u64 v[94:95], v[94:95], 2, v[90:91]
	global_load_dword v107, v[94:95], off
	s_ashr_i32 s54, s34, 7
	s_add_i32 s54, s54, s76
	s_lshl_b32 s54, s54, 1
	s_ashr_i32 s55, s54, 31
	s_lshl_b64 s[54:55], s[54:55], 2
	s_add_u32 s54, s60, s54
	s_addc_u32 s55, s61, s55
	global_load_dwordx2 v[94:95], v145, s[54:55]
	s_branch .LBB0_492
; #define LAS __attribute__((address_space(3)))
; #define LDS_BARRIER() do { asm volatile("s_waitcnt lgkmcnt(0)" ::: "memory"); __builtin_amdgcn_s_barrier(); asm volatile("" ::: "memory"); } while (0)
; __device__ __forceinline__ unsigned cvt_pk_bf16(float lo, float hi) { unsigned r; asm volatile("v_cvt_pk_bf16_f32 %0, %1, %2" : "=v"(r) : "v"(lo), "v"(hi)); return r; }
; __device__ __forceinline__ void p4_scan(const Args& a, const Frame& F) {
;     ...
;             auto commitK = [&](int kbuf) {
; #pragma unroll
;                 for (int i = 0; i < 8; ++i) { const int p = ht + 256 * i, row = p >> 4, c16 = p & 15; *(LAS u32x4*)(L + kbuf + row * SP + c16 * 16) = pk[i]; } };
;     ...
;             auto conv_store = [&]() {
;                 const bool hi = lane >= 32;
;                 u32x4 o[4];
; #pragma unroll
;                 for (int i = 0; i < 16; ++i) { const float snd = hi ? cv[i] : cv[16 + i]; const float rcv = __shfl_xor(snd, 32);
;                     const unsigned pkd = pg8::cvt_pk_bf16(hi ? rcv : cv[i], hi ? cv[16 + i] : rcv);
;                     if ((i & 3) == 0) o[i >> 2].x = pkd; else if ((i & 3) == 1) o[i >> 2].y = pkd; else if ((i & 3) == 2) o[i >> 2].z = pkd; else o[i >> 2].w = pkd; }
;                 u32x4* dst = (u32x4*)(cD + (size_t)crow * 1024 + ck0 + (hi ? 32 : 0));
; #pragma unroll
;                 for (int j2 = 0; j2 < 4; ++j2) dst[j2] = o[j2];
;             };
;     ...
;             for (int ci = 0; ci < 66; ++ci) {
;                 const float M127 = fmaxf(pmx, mcar), mnew = btot + M127;
;                 const int cnx = ci + 1 < 66 ? ci + 1 : 65;
;                 prefetch(cnx);
;                 commitK((ci & 1) ? S_K0 : S_K1);
;                 if (ci < 48) conv_store();
;                 conv_load(lw + 1024 * ((ci + 1) % 48));
;                 LDS_BARRIER();
;                 mcar = mnew;
;                 commitQ(); commitV(mcar, (ci & 1) ? S_VA0 : S_VA1); btot = pbt; pmx = ppx;
;                 LDS_BARRIER();
;             }
.LBB0_491:
	s_or_b64 exec, exec, s[54:55]
	v_mov_b64_e32 v[84:85], v[94:95]
	v_add_u32_e32 v8, s98, v104
	v_ashrrev_i32_e32 v9, 31, v8
	v_lshlrev_b64 v[10:11], 10, v[8:9]
	v_lshl_add_u64 v[10:11], v[86:87], 0, v[10:11]
	v_lshl_add_u64 v[8:9], v[8:9], 2, s[50:51]
	global_load_dwordx4 v[12:15], v[10:11], off
	global_load_dword v172, v[8:9], off
	v_add_u32_e32 v8, s98, v105
	v_ashrrev_i32_e32 v9, 31, v8
	v_lshlrev_b64 v[10:11], 10, v[8:9]
	v_lshl_add_u64 v[10:11], v[86:87], 0, v[10:11]
	v_lshl_add_u64 v[94:95], v[8:9], 2, s[50:51]
	global_load_dwordx4 v[8:11], v[10:11], off
	s_nop 0
	global_load_dword v171, v[94:95], off
	v_or_b32_e32 v94, s98, v106
	v_ashrrev_i32_e32 v95, 31, v94
	v_lshl_add_u64 v[190:191], v[94:95], 2, v[88:89]
	global_load_dword v108, v[190:191], off
	v_lshl_add_u64 v[94:95], v[94:95], 2, v[90:91]
	global_load_dword v107, v[94:95], off
	s_ashr_i32 s54, s98, 7
	s_add_i32 s54, s54, s76
	s_lshl_b32 s54, s54, 1
	s_ashr_i32 s55, s54, 31
	s_lshl_b64 s[54:55], s[54:55], 2
	s_add_u32 s54, s60, s54
	s_addc_u32 s55, s61, s55
	global_load_dwordx2 v[94:95], v145, s[54:55]
	s_waitcnt lgkmcnt(0)
	s_barrier
	s_cmpk_eq_i32 s35, 0x42
	s_mov_b32 s44, s35
	s_cbranch_scc1 .LBB0_434
.LBB0_492:
	s_waitcnt vmcnt(15)
	s_add_i32 s35, s44, 1
	s_bitcmp0_b32 s44, 0
	s_cselect_b64 s[54:55], -1, 0
	s_and_b64 s[56:57], s[54:55], exec
	s_cselect_b32 s56, 0x11000, s91
	s_add_i32 s56, s56, 0
	v_add3_u32 v144, s56, v109, v117
	ds_write_b128 v144, v[220:223]
	v_add3_u32 v48, s56, v110, v117
	ds_write_b128 v48, v[224:227]
	v_add3_u32 v48, s56, v111, v117
	ds_write_b128 v48, v[228:231]
	v_add3_u32 v48, s56, v112, v117
	ds_write_b128 v48, v[232:235]
	v_add3_u32 v48, s56, v113, v117
	ds_write_b128 v48, v[236:239]
	v_add3_u32 v48, s56, v114, v117
	ds_write_b128 v48, v[240:243]
	v_add3_u32 v48, s56, v115, v117
	ds_write_b128 v48, v[244:247]
	v_add3_u32 v48, s56, v116, v117
	s_cmp_gt_u32 s44, 47
	ds_write_b128 v48, v[248:251]
	s_cbranch_scc1 .LBB0_498
	v_permlane32_swap_b32_e32 v148, v183
	v_cvt_pk_bf16_f32 v48, v148, v183
	v_permlane32_swap_b32_e32 v141, v179
	v_cvt_pk_bf16_f32 v49, v141, v179
	v_permlane32_swap_b32_e32 v149, v184
	v_cvt_pk_bf16_f32 v50, v149, v184
	v_permlane32_swap_b32_e32 v137, v175
	v_cvt_pk_bf16_f32 v51, v137, v175
	v_permlane32_swap_b32_e32 v142, v180
	v_cvt_pk_bf16_f32 v52, v142, v180
	v_permlane32_swap_b32_e32 v81, v173
	v_cvt_pk_bf16_f32 v53, v81, v173
	v_permlane32_swap_b32_e32 v138, v176
	v_ashrrev_i32_e32 v81, 31, v80
	v_cvt_pk_bf16_f32 v54, v138, v176
	v_permlane32_swap_b32_e32 v151, v186
	v_cvt_pk_bf16_f32 v55, v151, v186
	v_permlane32_swap_b32_e32 v152, v187
	v_cvt_pk_bf16_f32 v56, v152, v187
	v_permlane32_swap_b32_e32 v143, v181
	v_cvt_pk_bf16_f32 v57, v143, v181
	v_permlane32_swap_b32_e32 v150, v185
	v_cvt_pk_bf16_f32 v58, v150, v185
	v_permlane32_swap_b32_e32 v139, v177
	v_cvt_pk_bf16_f32 v59, v139, v177
	v_permlane32_swap_b32_e32 v147, v182
	v_cvt_pk_bf16_f32 v60, v147, v182
	v_permlane32_swap_b32_e32 v83, v174
	v_mov_b32_e32 v147, v145
	v_cvt_pk_bf16_f32 v61, v83, v174
	v_permlane32_swap_b32_e32 v140, v178
	v_mov_b32_e32 v83, v145
	v_cvt_pk_bf16_f32 v62, v140, v178
	v_permlane32_swap_b32_e32 v153, v188
	v_cvt_pk_bf16_f32 v63, v153, v188
	v_lshlrev_b64 v[64:65], 11, v[80:81]
	v_lshl_add_u64 v[64:65], s[52:53], 0, v[64:65]
	v_lshl_add_u64 v[64:65], v[82:83], 1, v[64:65]
	v_lshl_add_u64 v[64:65], v[64:65], 0, v[146:147]
	global_store_dwordx4 v[64:65], v[48:51], off
	global_store_dwordx4 v[64:65], v[52:55], off offset:16
	global_store_dwordx4 v[64:65], v[56:59], off offset:32
	global_store_dwordx4 v[64:65], v[60:63], off offset:48
